# baseline (speedup 1.0000x reference)
.LBB0_24:
	s_setprio 1
	s_waitcnt lgkmcnt(14)
	v_mfma_f32_32x32x16_f16 v[50:65], v[142:145], v[158:161], v[50:65]
	v_exp_f32_e32 v18, v18
	v_exp_f32_e32 v19, v19
	v_exp_f32_e32 v20, v20
	v_exp_f32_e32 v21, v21
	s_waitcnt lgkmcnt(12)
	v_mfma_f32_32x32x16_f16 v[66:81], v[138:141], v[158:161], v[66:81]
	v_exp_f32_e32 v22, v22
	v_exp_f32_e32 v23, v23
	v_exp_f32_e32 v24, v24
	v_exp_f32_e32 v25, v25
	v_add_u32_e32 v2, s77, v230
	ds_read_b128 v[90:93], v2
	ds_read_b128 v[182:185], v2 offset:4096
	s_waitcnt lgkmcnt(12)
	v_mfma_f32_32x32x16_f16 v[50:65], v[134:137], v[154:157], v[50:65]
	v_exp_f32_e32 v26, v26
	v_exp_f32_e32 v27, v27
	v_exp_f32_e32 v28, v28
	v_exp_f32_e32 v29, v29
	v_add_u32_e32 v2, s77, v231
	ds_read_b128 v[202:205], v2
	ds_read_b128 v[178:181], v2 offset:4096
	s_waitcnt lgkmcnt(12)
	v_mfma_f32_32x32x16_f16 v[66:81], v[106:109], v[154:157], v[66:81]
	v_exp_f32_e32 v30, v30
	v_exp_f32_e32 v31, v31
	v_exp_f32_e32 v32, v32
	v_exp_f32_e32 v33, v33
	v_add_u32_e32 v2, s77, v232
	ds_read_b128 v[198:201], v2
	ds_read_b128 v[138:141], v2 offset:4096
	s_waitcnt lgkmcnt(12)
	v_mfma_f32_32x32x16_f16 v[50:65], v[102:105], v[150:153], v[50:65]
	v_exp_f32_e32 v34, v34
	v_exp_f32_e32 v35, v35
	v_exp_f32_e32 v36, v36
	v_exp_f32_e32 v37, v37
	v_add_u32_e32 v2, s77, v233
	ds_read_b128 v[142:145], v2
	ds_read_b128 v[134:137], v2 offset:4096
	s_waitcnt lgkmcnt(12)
	v_mfma_f32_32x32x16_f16 v[66:81], v[98:101], v[150:153], v[66:81]
	v_exp_f32_e32 v38, v38
	v_exp_f32_e32 v39, v39
	v_exp_f32_e32 v40, v40
	v_exp_f32_e32 v41, v41
	s_waitcnt lgkmcnt(10)
	v_mfma_f32_32x32x16_f16 v[50:65], v[86:89], v[146:149], v[50:65]
	v_exp_f32_e32 v42, v42
	v_exp_f32_e32 v43, v43
	v_exp_f32_e32 v44, v44
	v_exp_f32_e32 v45, v45
	s_waitcnt lgkmcnt(8)
	v_mfma_f32_32x32x16_f16 v[66:81], v[82:85], v[146:149], v[66:81]
	v_exp_f32_e32 v46, v46
	v_exp_f32_e32 v47, v47
	v_exp_f32_e32 v48, v48
	v_exp_f32_e32 v49, v49
	s_setprio 0
	s_waitcnt vmcnt(3)
	v_cvt_pkrtz_f16_f32 v8, v8, v9
	v_cvt_pkrtz_f16_f32 v9, v10, v11
	v_add_u32_e32 v83, s97, v249
	s_waitcnt vmcnt(2)
	v_cvt_pkrtz_f16_f32 v4, v4, v5
	v_cvt_pkrtz_f16_f32 v5, v6, v7
	ds_write2st64_b64 v83, v[8:9], v[4:5] offset1:8
	s_waitcnt vmcnt(1)
	v_cvt_pkrtz_f16_f32 v84, v130, v131
	v_cvt_pkrtz_f16_f32 v85, v132, v133
	s_waitcnt vmcnt(0)
	v_cvt_pkrtz_f16_f32 v86, v12, v13
	v_cvt_pkrtz_f16_f32 v87, v14, v15
	s_andn2_b64 vcc, exec, s[4:5]
	ds_write2st64_b64 v250, v[84:85], v[86:87] offset0:64 offset1:68
	s_add_i32 s98, s98, 2
	s_min_i32 s4, s98, s95
	s_lshl_b32 s5, s4, 18
	s_add_u32 s18, s100, s5
	s_addc_u32 s19, s101, 0
	s_add_i32 s5, s98, -1
	s_lshl_b32 s5, s5, 18
	s_add_u32 s20, s0, s5
	s_addc_u32 s21, s1, 0
	s_cmp_eq_u32 s4, s95
	s_cbranch_scc1 .Lclamp2
	global_load_dwordx4 v[8:11], v245, s[18:19]
	global_load_dwordx4 v[4:7], v246, s[18:19]
	global_load_dwordx4 v[210:213], v245, s[20:21]
	global_load_dwordx4 v[12:15], v246, s[20:21]
.Lloads2_done:
	s_waitcnt lgkmcnt(0)
	s_barrier
	s_cbranch_vccnz .LBB0_26
	v_pk_mul_f32 v[64:65], v[228:229], v[64:65] op_sel_hi:[0,1]
	v_pk_mul_f32 v[62:63], v[228:229], v[62:63] op_sel_hi:[0,1]
	v_pk_mul_f32 v[60:61], v[228:229], v[60:61] op_sel_hi:[0,1]
	v_pk_mul_f32 v[58:59], v[228:229], v[58:59] op_sel_hi:[0,1]
	v_pk_mul_f32 v[56:57], v[228:229], v[56:57] op_sel_hi:[0,1]
	v_pk_mul_f32 v[54:55], v[228:229], v[54:55] op_sel_hi:[0,1]
	v_pk_mul_f32 v[52:53], v[228:229], v[52:53] op_sel_hi:[0,1]
	v_pk_mul_f32 v[50:51], v[228:229], v[50:51] op_sel_hi:[0,1]
	v_pk_mul_f32 v[80:81], v[228:229], v[80:81] op_sel_hi:[0,1]
	v_pk_mul_f32 v[78:79], v[228:229], v[78:79] op_sel_hi:[0,1]
	v_pk_mul_f32 v[76:77], v[228:229], v[76:77] op_sel_hi:[0,1]
	v_pk_mul_f32 v[74:75], v[228:229], v[74:75] op_sel_hi:[0,1]
	v_pk_mul_f32 v[72:73], v[228:229], v[72:73] op_sel_hi:[0,1]
	v_pk_mul_f32 v[70:71], v[228:229], v[70:71] op_sel_hi:[0,1]
	v_pk_mul_f32 v[68:69], v[228:229], v[68:69] op_sel_hi:[0,1]
	v_pk_mul_f32 v[66:67], v[228:229], v[66:67] op_sel_hi:[0,1]

.Lclamp2:
	s_lshl_b32 s5, s4, 6
	s_sub_i32 s5, s96, s5
	v_lshrrev_b32_e32 v94, 4, v0
	v_and_b32_e32 v95, 15, v0
	v_lshlrev_b32_e32 v95, 4, v95
	v_min_i32_e32 v96, s5, v94
	v_lshl_add_u32 v96, v96, 12, v95
	global_load_dwordx4 v[8:11], v96, s[18:19]
	v_add_u32_e32 v96, 32, v94
	v_min_i32_e32 v96, s5, v96
	v_lshl_add_u32 v96, v96, 12, v95
	global_load_dwordx4 v[4:7], v96, s[18:19]
	s_lshl_b32 s5, s98, 6
	s_sub_i32 s5, s96, s5
	s_add_i32 s5, s5, 128
	v_min_i32_e32 v96, s5, v94
	v_lshl_add_u32 v96, v96, 12, v95
	global_load_dwordx4 v[210:213], v96, s[20:21]
	v_add_u32_e32 v96, 32, v94
	v_min_i32_e32 v96, s5, v96
	v_lshl_add_u32 v96, v96, 12, v95
	global_load_dwordx4 v[12:15], v96, s[20:21]
	s_branch .Lloads2_done
